# baseline (speedup 1.0000x reference)
_Z8dog_mainPKfS0_S0_S0_S0_S0_S0_Pf:
	s_load_dwordx8 s[12:19], s[0:1], 0x0
	s_load_dwordx8 s[20:27], s[0:1], 0x20
	s_and_b32 s3, s2, 7
	s_lshl_b32 s3, s3, 5
	s_lshr_b32 s4, s2, 3
	s_add_i32 s4, s3, s4
	s_and_b32 s6, s4, 3
	s_lshr_b32 s7, s4, 2
	s_mov_b32 s5, 0
	s_lshl_b64 s[8:9], s[4:5], 18
	v_and_b32_e32 v1, 63, v0
	v_lshrrev_b32_e32 v2, 6, v0
	v_and_b32_e32 v3, 15, v0
	v_and_b32_e32 v7, 31, v0
	v_lshl_or_b32 v5, v2, 5, v7
	v_lshlrev_b32_e32 v5, 2, v5
	v_mov_b32_e32 v4, v5
	v_lshlrev_b32_e32 v6, 4, v1
	v_lshl_or_b32 v6, v2, 12, v6
	v_bfe_u32 v7, v0, 4, 2
	s_waitcnt lgkmcnt(0)
	global_load_dword v32, v4, s[18:19]
	global_load_dword v33, v4, s[20:21]
	global_load_dword v34, v4, s[22:23]
	global_load_dword v35, v4, s[24:25]
	global_load_dword v36, v4, s[14:15]
	global_load_dword v37, v4, s[16:17]
	s_add_u32 s12, s12, s8
	s_addc_u32 s13, s13, s9
	global_load_dwordx4 v[128:131], v6, s[12:13] offset:0 nt
	global_load_dwordx4 v[132:135], v6, s[12:13] offset:1024 nt
	global_load_dwordx4 v[136:139], v6, s[12:13] offset:2048 nt
	global_load_dwordx4 v[140:143], v6, s[12:13] offset:3072 nt
	v_add_u32_e32 v6, 0x8000, v6
	global_load_dwordx4 v[144:147], v6, s[12:13] offset:0 nt
	global_load_dwordx4 v[148:151], v6, s[12:13] offset:1024 nt
	global_load_dwordx4 v[152:155], v6, s[12:13] offset:2048 nt
	global_load_dwordx4 v[156:159], v6, s[12:13] offset:3072 nt
	v_and_b32_e32 v16, 1, v0
	v_cmp_eq_u32_e64 s[30:31], 0, v16
	v_and_b32_e32 v17, 2, v0
	v_cmp_eq_u32_e64 s[32:33], 0, v17
	v_and_b32_e32 v16, 3, v0
	v_lshrrev_b32_e32 v17, 2, v1
	v_lshlrev_b32_e32 v16, 5, v16
	v_lshl_add_u32 v16, v17, 1, v16
	v_lshrrev_b32_e32 v17, 1, v2
	s_movk_i32 s10, 0x110
	v_mad_u32_u24 v16, v17, s10, v16
	v_and_b32_e32 v17, 1, v2
	v_lshl_add_u32 v14, v17, 7, v16
	v_lshlrev_b32_e32 v17, 4, v7
	v_mad_u32_u24 v15, v3, s10, v17
	s_lshl_b32 s11, s6, 5
	v_lshl_add_u32 v18, v7, 2, s11
	v_cvt_f32_u32_e32 v18, v18
	v_lshlrev_b32_e32 v19, 3, v7
	v_cvt_f32_u32_e32 v19, v19
	s_mov_b32 s29, 2
	s_branch .Lpass
.Ldry_done:
	s_waitcnt vmcnt(8)
	v_lshlrev_b32_e32 v16, 2, v3
	v_add_u32_e32 v17, 64, v16
	ds_bpermute_b32 v40, v16, v32
	ds_bpermute_b32 v46, v17, v32
	ds_bpermute_b32 v41, v16, v33
	ds_bpermute_b32 v47, v17, v33
	ds_bpermute_b32 v42, v16, v34
	ds_bpermute_b32 v48, v17, v34
	ds_bpermute_b32 v43, v16, v35
	ds_bpermute_b32 v49, v17, v35
	ds_bpermute_b32 v44, v16, v36
	ds_bpermute_b32 v50, v17, v36
	ds_bpermute_b32 v45, v16, v37
	ds_bpermute_b32 v51, v17, v37
	s_waitcnt lgkmcnt(0)
	v_add_f32_e32 v41, v40, v41
	v_sub_f32_e32 v12, v19, v42
	v_sub_f32_e32 v13, v18, v43
	v_rcp_f32_e32 v42, v40
	v_rcp_f32_e32 v43, v41
	s_nop 0
	v_fma_f32 v20, -v40, v42, 1.0
	v_fma_f32 v42, v20, v42, v42
	v_fma_f32 v20, -v41, v43, 1.0
	v_fma_f32 v43, v20, v43, v43
	v_mul_f32_e32 v8, 0xbf38aa3b, v42
	v_mul_f32_e32 v9, 0xbf38aa3b, v43
	v_mul_f32_e32 v44, v44, v42
	v_mul_f32_e32 v45, v45, v43
	v_mul_f32_e32 v10, 0x3e22f983, v44
	v_mul_f32_e32 v11, 0x3e22f983, v45
	v_add_f32_e32 v47, v46, v47
	v_sub_f32_e32 v2, v19, v48
	v_sub_f32_e32 v3, v18, v49
	v_rcp_f32_e32 v48, v46
	v_rcp_f32_e32 v49, v47
	s_nop 0
	v_fma_f32 v20, -v46, v48, 1.0
	v_fma_f32 v48, v20, v48, v48
	v_fma_f32 v20, -v47, v49, 1.0
	v_fma_f32 v49, v20, v49, v49
	v_mul_f32_e32 v28, 0xbf38aa3b, v48
	v_mul_f32_e32 v29, 0xbf38aa3b, v49
	v_mul_f32_e32 v50, v50, v48
	v_mul_f32_e32 v51, v51, v49
	v_mul_f32_e32 v30, 0x3e22f983, v50
	v_mul_f32_e32 v31, 0x3e22f983, v51
	s_getpc_b64 s[44:45]

.Lno_karg_touch:
	v_mul_f32_e32 v16, v12, v12
	v_add_f32_e32 v17, 0x3f800000, v12
	v_add_f32_e32 v18, 0x40000000, v12
	v_add_f32_e32 v19, 0x40400000, v12
	v_mul_f32_e32 v17, v17, v17
	v_mul_f32_e32 v18, v18, v18
	v_mul_f32_e32 v19, v19, v19
	v_mul_f32_e32 v20, v8, v16
	v_mul_f32_e32 v24, v9, v16
	v_mul_f32_e32 v21, v8, v17
	v_mul_f32_e32 v25, v9, v17
	v_mul_f32_e32 v22, v8, v18
	v_mul_f32_e32 v26, v9, v18
	v_mul_f32_e32 v23, v8, v19
	v_mul_f32_e32 v27, v9, v19
	v_exp_f32_e32 v20, v20
	v_exp_f32_e32 v21, v21
	v_exp_f32_e32 v22, v22
	v_exp_f32_e32 v23, v23
	v_exp_f32_e32 v24, v24
	v_exp_f32_e32 v25, v25
	v_exp_f32_e32 v26, v26
	v_exp_f32_e32 v27, v27
	v_cvt_pk_f16_f32 v32, v20, v21
	v_cvt_pk_f16_f32 v33, v22, v23
	v_cvt_pk_f16_f32 v64, v24, v25
	v_cvt_pk_f16_f32 v65, v26, v27
	v_add_f32_e32 v16, 0x40800000, v12
	v_add_f32_e32 v17, 0x40a00000, v12
	v_add_f32_e32 v18, 0x40c00000, v12
	v_add_f32_e32 v19, 0x40e00000, v12
	v_mul_f32_e32 v16, v16, v16
	v_mul_f32_e32 v17, v17, v17
	v_mul_f32_e32 v18, v18, v18
	v_mul_f32_e32 v19, v19, v19
	v_mul_f32_e32 v20, v8, v16
	v_mul_f32_e32 v24, v9, v16
	v_mul_f32_e32 v21, v8, v17
	v_mul_f32_e32 v25, v9, v17
	v_mul_f32_e32 v22, v8, v18
	v_mul_f32_e32 v26, v9, v18
	v_mul_f32_e32 v23, v8, v19
	v_mul_f32_e32 v27, v9, v19
	v_exp_f32_e32 v20, v20
	v_exp_f32_e32 v21, v21
	v_exp_f32_e32 v22, v22
	v_exp_f32_e32 v23, v23
	v_exp_f32_e32 v24, v24
	v_exp_f32_e32 v25, v25
	v_exp_f32_e32 v26, v26
	v_exp_f32_e32 v27, v27
	v_cvt_pk_f16_f32 v34, v20, v21
	v_cvt_pk_f16_f32 v35, v22, v23
	v_cvt_pk_f16_f32 v66, v24, v25
	v_cvt_pk_f16_f32 v67, v26, v27
	v_add_f32_e32 v16, 0x42000000, v12
	v_add_f32_e32 v17, 0x42040000, v12
	v_add_f32_e32 v18, 0x42080000, v12
	v_add_f32_e32 v19, 0x420c0000, v12
	v_mul_f32_e32 v16, v16, v16
	v_mul_f32_e32 v17, v17, v17
	v_mul_f32_e32 v18, v18, v18
	v_mul_f32_e32 v19, v19, v19
	v_mul_f32_e32 v20, v8, v16
	v_mul_f32_e32 v24, v9, v16
	v_mul_f32_e32 v21, v8, v17
	v_mul_f32_e32 v25, v9, v17
	v_mul_f32_e32 v22, v8, v18
	v_mul_f32_e32 v26, v9, v18
	v_mul_f32_e32 v23, v8, v19
	v_mul_f32_e32 v27, v9, v19
	v_exp_f32_e32 v20, v20
	v_exp_f32_e32 v21, v21
	v_exp_f32_e32 v22, v22
	v_exp_f32_e32 v23, v23
	v_exp_f32_e32 v24, v24
	v_exp_f32_e32 v25, v25
	v_exp_f32_e32 v26, v26
	v_exp_f32_e32 v27, v27
	v_cvt_pk_f16_f32 v36, v20, v21
	v_cvt_pk_f16_f32 v37, v22, v23
	v_cvt_pk_f16_f32 v68, v24, v25
	v_cvt_pk_f16_f32 v69, v26, v27
	v_add_f32_e32 v16, 0x42100000, v12
	v_add_f32_e32 v17, 0x42140000, v12
	v_add_f32_e32 v18, 0x42180000, v12
	v_add_f32_e32 v19, 0x421c0000, v12
	v_mul_f32_e32 v16, v16, v16
	v_mul_f32_e32 v17, v17, v17
	v_mul_f32_e32 v18, v18, v18
	v_mul_f32_e32 v19, v19, v19
	v_mul_f32_e32 v20, v8, v16
	v_mul_f32_e32 v24, v9, v16
	v_mul_f32_e32 v21, v8, v17
	v_mul_f32_e32 v25, v9, v17
	v_mul_f32_e32 v22, v8, v18
	v_mul_f32_e32 v26, v9, v18
	v_mul_f32_e32 v23, v8, v19
	v_mul_f32_e32 v27, v9, v19
	v_exp_f32_e32 v20, v20
	v_exp_f32_e32 v21, v21
	v_exp_f32_e32 v22, v22
	v_exp_f32_e32 v23, v23
	v_exp_f32_e32 v24, v24
	v_exp_f32_e32 v25, v25
	v_exp_f32_e32 v26, v26
	v_exp_f32_e32 v27, v27
	v_cvt_pk_f16_f32 v38, v20, v21
	v_cvt_pk_f16_f32 v39, v22, v23
	v_cvt_pk_f16_f32 v70, v24, v25
	v_cvt_pk_f16_f32 v71, v26, v27
	v_add_u32_e32 v6, 0x8000, v6
	global_load_dwordx4 v[160:163], v6, s[12:13] offset:0 nt
	global_load_dwordx4 v[164:167], v6, s[12:13] offset:1024 nt
	global_load_dwordx4 v[168:171], v6, s[12:13] offset:2048 nt
	global_load_dwordx4 v[172:175], v6, s[12:13] offset:3072 nt
	v_add_f32_e32 v16, 0x42800000, v12
	v_add_f32_e32 v17, 0x42820000, v12
	v_add_f32_e32 v18, 0x42840000, v12
	v_add_f32_e32 v19, 0x42860000, v12
	v_mul_f32_e32 v16, v16, v16
	v_mul_f32_e32 v17, v17, v17
	v_mul_f32_e32 v18, v18, v18
	v_mul_f32_e32 v19, v19, v19
	v_mul_f32_e32 v20, v8, v16
	v_mul_f32_e32 v24, v9, v16
	v_mul_f32_e32 v21, v8, v17
	v_mul_f32_e32 v25, v9, v17
	v_mul_f32_e32 v22, v8, v18
	v_mul_f32_e32 v26, v9, v18
	v_mul_f32_e32 v23, v8, v19
	v_mul_f32_e32 v27, v9, v19
	v_exp_f32_e32 v20, v20
	v_exp_f32_e32 v21, v21
	v_exp_f32_e32 v22, v22
	v_exp_f32_e32 v23, v23
	v_exp_f32_e32 v24, v24
	v_exp_f32_e32 v25, v25
	v_exp_f32_e32 v26, v26
	v_exp_f32_e32 v27, v27
	v_cvt_pk_f16_f32 v40, v20, v21
	v_cvt_pk_f16_f32 v41, v22, v23
	v_cvt_pk_f16_f32 v72, v24, v25
	v_cvt_pk_f16_f32 v73, v26, v27
	v_add_f32_e32 v16, 0x42880000, v12
	v_add_f32_e32 v17, 0x428a0000, v12
	v_add_f32_e32 v18, 0x428c0000, v12
	v_add_f32_e32 v19, 0x428e0000, v12
	v_mul_f32_e32 v16, v16, v16
	v_mul_f32_e32 v17, v17, v17
	v_mul_f32_e32 v18, v18, v18
	v_mul_f32_e32 v19, v19, v19
	v_mul_f32_e32 v20, v8, v16
	v_mul_f32_e32 v24, v9, v16
	v_mul_f32_e32 v21, v8, v17
	v_mul_f32_e32 v25, v9, v17
	v_mul_f32_e32 v22, v8, v18
	v_mul_f32_e32 v26, v9, v18
	v_mul_f32_e32 v23, v8, v19
	v_mul_f32_e32 v27, v9, v19
	v_exp_f32_e32 v20, v20
	v_exp_f32_e32 v21, v21
	v_exp_f32_e32 v22, v22
	v_exp_f32_e32 v23, v23
	v_exp_f32_e32 v24, v24
	v_exp_f32_e32 v25, v25
	v_exp_f32_e32 v26, v26
	v_exp_f32_e32 v27, v27
	v_cvt_pk_f16_f32 v42, v20, v21
	v_cvt_pk_f16_f32 v43, v22, v23
	v_cvt_pk_f16_f32 v74, v24, v25
	v_cvt_pk_f16_f32 v75, v26, v27
	v_add_f32_e32 v16, 0x42c00000, v12
	v_add_f32_e32 v17, 0x42c20000, v12
	v_add_f32_e32 v18, 0x42c40000, v12
	v_add_f32_e32 v19, 0x42c60000, v12
	v_mul_f32_e32 v16, v16, v16
	v_mul_f32_e32 v17, v17, v17
	v_mul_f32_e32 v18, v18, v18
	v_mul_f32_e32 v19, v19, v19
	v_mul_f32_e32 v20, v8, v16
	v_mul_f32_e32 v24, v9, v16
	v_mul_f32_e32 v21, v8, v17
	v_mul_f32_e32 v25, v9, v17
	v_mul_f32_e32 v22, v8, v18
	v_mul_f32_e32 v26, v9, v18
	v_mul_f32_e32 v23, v8, v19
	v_mul_f32_e32 v27, v9, v19
	v_exp_f32_e32 v20, v20
	v_exp_f32_e32 v21, v21
	v_exp_f32_e32 v22, v22
	v_exp_f32_e32 v23, v23
	v_exp_f32_e32 v24, v24
	v_exp_f32_e32 v25, v25
	v_exp_f32_e32 v26, v26
	v_exp_f32_e32 v27, v27
	v_cvt_pk_f16_f32 v44, v20, v21
	v_cvt_pk_f16_f32 v45, v22, v23
	v_cvt_pk_f16_f32 v76, v24, v25
	v_cvt_pk_f16_f32 v77, v26, v27
	v_add_f32_e32 v16, 0x42c80000, v12
	v_add_f32_e32 v17, 0x42ca0000, v12
	v_add_f32_e32 v18, 0x42cc0000, v12
	v_add_f32_e32 v19, 0x42ce0000, v12
	v_mul_f32_e32 v16, v16, v16
	v_mul_f32_e32 v17, v17, v17
	v_mul_f32_e32 v18, v18, v18
	v_mul_f32_e32 v19, v19, v19
	v_mul_f32_e32 v20, v8, v16
	v_mul_f32_e32 v24, v9, v16
	v_mul_f32_e32 v21, v8, v17
	v_mul_f32_e32 v25, v9, v17
	v_mul_f32_e32 v22, v8, v18
	v_mul_f32_e32 v26, v9, v18
	v_mul_f32_e32 v23, v8, v19
	v_mul_f32_e32 v27, v9, v19
	v_exp_f32_e32 v20, v20
	v_exp_f32_e32 v21, v21
	v_exp_f32_e32 v22, v22
	v_exp_f32_e32 v23, v23
	v_exp_f32_e32 v24, v24
	v_exp_f32_e32 v25, v25
	v_exp_f32_e32 v26, v26
	v_exp_f32_e32 v27, v27
	v_cvt_pk_f16_f32 v46, v20, v21
	v_cvt_pk_f16_f32 v47, v22, v23
	v_cvt_pk_f16_f32 v78, v24, v25
	v_cvt_pk_f16_f32 v79, v26, v27
	v_add_u32_e32 v6, 0x8000, v6
	global_load_dwordx4 v[176:179], v6, s[12:13] offset:0 nt
	global_load_dwordx4 v[180:183], v6, s[12:13] offset:1024 nt
	global_load_dwordx4 v[184:187], v6, s[12:13] offset:2048 nt
	global_load_dwordx4 v[188:191], v6, s[12:13] offset:3072 nt
	v_mul_f32_e32 v16, v2, v2
	v_add_f32_e32 v17, 0x3f800000, v2
	v_add_f32_e32 v18, 0x40000000, v2
	v_add_f32_e32 v19, 0x40400000, v2
	v_mul_f32_e32 v17, v17, v17
	v_mul_f32_e32 v18, v18, v18
	v_mul_f32_e32 v19, v19, v19
	v_mul_f32_e32 v20, v28, v16
	v_mul_f32_e32 v24, v29, v16
	v_mul_f32_e32 v21, v28, v17
	v_mul_f32_e32 v25, v29, v17
	v_mul_f32_e32 v22, v28, v18
	v_mul_f32_e32 v26, v29, v18
	v_mul_f32_e32 v23, v28, v19
	v_mul_f32_e32 v27, v29, v19
	v_exp_f32_e32 v20, v20
	v_exp_f32_e32 v21, v21
	v_exp_f32_e32 v22, v22
	v_exp_f32_e32 v23, v23
	v_exp_f32_e32 v24, v24
	v_exp_f32_e32 v25, v25
	v_exp_f32_e32 v26, v26
	v_exp_f32_e32 v27, v27
	v_cvt_pk_f16_f32 v48, v20, v21
	v_cvt_pk_f16_f32 v49, v22, v23
	v_cvt_pk_f16_f32 v80, v24, v25
	v_cvt_pk_f16_f32 v81, v26, v27
	v_add_f32_e32 v16, 0x40800000, v2
	v_add_f32_e32 v17, 0x40a00000, v2
	v_add_f32_e32 v18, 0x40c00000, v2
	v_add_f32_e32 v19, 0x40e00000, v2
	v_mul_f32_e32 v16, v16, v16
	v_mul_f32_e32 v17, v17, v17
	v_mul_f32_e32 v18, v18, v18
	v_mul_f32_e32 v19, v19, v19
	v_mul_f32_e32 v20, v28, v16
	v_mul_f32_e32 v24, v29, v16
	v_mul_f32_e32 v21, v28, v17
	v_mul_f32_e32 v25, v29, v17
	v_mul_f32_e32 v22, v28, v18
	v_mul_f32_e32 v26, v29, v18
	v_mul_f32_e32 v23, v28, v19
	v_mul_f32_e32 v27, v29, v19
	v_exp_f32_e32 v20, v20
	v_exp_f32_e32 v21, v21
	v_exp_f32_e32 v22, v22
	v_exp_f32_e32 v23, v23
	v_exp_f32_e32 v24, v24
	v_exp_f32_e32 v25, v25
	v_exp_f32_e32 v26, v26
	v_exp_f32_e32 v27, v27
	v_cvt_pk_f16_f32 v50, v20, v21
	v_cvt_pk_f16_f32 v51, v22, v23
	v_cvt_pk_f16_f32 v82, v24, v25
	v_cvt_pk_f16_f32 v83, v26, v27
	v_add_f32_e32 v16, 0x42000000, v2
	v_add_f32_e32 v17, 0x42040000, v2
	v_add_f32_e32 v18, 0x42080000, v2
	v_add_f32_e32 v19, 0x420c0000, v2
	v_mul_f32_e32 v16, v16, v16
	v_mul_f32_e32 v17, v17, v17
	v_mul_f32_e32 v18, v18, v18
	v_mul_f32_e32 v19, v19, v19
	v_mul_f32_e32 v20, v28, v16
	v_mul_f32_e32 v24, v29, v16
	v_mul_f32_e32 v21, v28, v17
	v_mul_f32_e32 v25, v29, v17
	v_mul_f32_e32 v22, v28, v18
	v_mul_f32_e32 v26, v29, v18
	v_mul_f32_e32 v23, v28, v19
	v_mul_f32_e32 v27, v29, v19
	v_exp_f32_e32 v20, v20
	v_exp_f32_e32 v21, v21
	v_exp_f32_e32 v22, v22
	v_exp_f32_e32 v23, v23
	v_exp_f32_e32 v24, v24
	v_exp_f32_e32 v25, v25
	v_exp_f32_e32 v26, v26
	v_exp_f32_e32 v27, v27
	v_cvt_pk_f16_f32 v52, v20, v21
	v_cvt_pk_f16_f32 v53, v22, v23
	v_cvt_pk_f16_f32 v84, v24, v25
	v_cvt_pk_f16_f32 v85, v26, v27
	v_add_f32_e32 v16, 0x42100000, v2
	v_add_f32_e32 v17, 0x42140000, v2
	v_add_f32_e32 v18, 0x42180000, v2
	v_add_f32_e32 v19, 0x421c0000, v2
	v_mul_f32_e32 v16, v16, v16
	v_mul_f32_e32 v17, v17, v17
	v_mul_f32_e32 v18, v18, v18
	v_mul_f32_e32 v19, v19, v19
	v_mul_f32_e32 v20, v28, v16
	v_mul_f32_e32 v24, v29, v16
	v_mul_f32_e32 v21, v28, v17
	v_mul_f32_e32 v25, v29, v17
	v_mul_f32_e32 v22, v28, v18
	v_mul_f32_e32 v26, v29, v18
	v_mul_f32_e32 v23, v28, v19
	v_mul_f32_e32 v27, v29, v19
	v_exp_f32_e32 v20, v20
	v_exp_f32_e32 v21, v21
	v_exp_f32_e32 v22, v22
	v_exp_f32_e32 v23, v23
	v_exp_f32_e32 v24, v24
	v_exp_f32_e32 v25, v25
	v_exp_f32_e32 v26, v26
	v_exp_f32_e32 v27, v27
	v_cvt_pk_f16_f32 v54, v20, v21
	v_cvt_pk_f16_f32 v55, v22, v23
	v_cvt_pk_f16_f32 v86, v24, v25
	v_cvt_pk_f16_f32 v87, v26, v27
	v_add_u32_e32 v6, 0x8000, v6
	global_load_dwordx4 v[192:195], v6, s[12:13] offset:0 nt
	global_load_dwordx4 v[196:199], v6, s[12:13] offset:1024 nt
	global_load_dwordx4 v[200:203], v6, s[12:13] offset:2048 nt
	global_load_dwordx4 v[204:207], v6, s[12:13] offset:3072 nt
	v_add_f32_e32 v16, 0x42800000, v2
	v_add_f32_e32 v17, 0x42820000, v2
	v_add_f32_e32 v18, 0x42840000, v2
	v_add_f32_e32 v19, 0x42860000, v2
	v_mul_f32_e32 v16, v16, v16
	v_mul_f32_e32 v17, v17, v17
	v_mul_f32_e32 v18, v18, v18
	v_mul_f32_e32 v19, v19, v19
	v_mul_f32_e32 v20, v28, v16
	v_mul_f32_e32 v24, v29, v16
	v_mul_f32_e32 v21, v28, v17
	v_mul_f32_e32 v25, v29, v17
	v_mul_f32_e32 v22, v28, v18
	v_mul_f32_e32 v26, v29, v18
	v_mul_f32_e32 v23, v28, v19
	v_mul_f32_e32 v27, v29, v19
	v_exp_f32_e32 v20, v20
	v_exp_f32_e32 v21, v21
	v_exp_f32_e32 v22, v22
	v_exp_f32_e32 v23, v23
	v_exp_f32_e32 v24, v24
	v_exp_f32_e32 v25, v25
	v_exp_f32_e32 v26, v26
	v_exp_f32_e32 v27, v27
	v_cvt_pk_f16_f32 v56, v20, v21
	v_cvt_pk_f16_f32 v57, v22, v23
	v_cvt_pk_f16_f32 v88, v24, v25
	v_cvt_pk_f16_f32 v89, v26, v27
	v_add_f32_e32 v16, 0x42880000, v2
	v_add_f32_e32 v17, 0x428a0000, v2
	v_add_f32_e32 v18, 0x428c0000, v2
	v_add_f32_e32 v19, 0x428e0000, v2
	v_mul_f32_e32 v16, v16, v16
	v_mul_f32_e32 v17, v17, v17
	v_mul_f32_e32 v18, v18, v18
	v_mul_f32_e32 v19, v19, v19
	v_mul_f32_e32 v20, v28, v16
	v_mul_f32_e32 v24, v29, v16
	v_mul_f32_e32 v21, v28, v17
	v_mul_f32_e32 v25, v29, v17
	v_mul_f32_e32 v22, v28, v18
	v_mul_f32_e32 v26, v29, v18
	v_mul_f32_e32 v23, v28, v19
	v_mul_f32_e32 v27, v29, v19
	v_exp_f32_e32 v20, v20
	v_exp_f32_e32 v21, v21
	v_exp_f32_e32 v22, v22
	v_exp_f32_e32 v23, v23
	v_exp_f32_e32 v24, v24
	v_exp_f32_e32 v25, v25
	v_exp_f32_e32 v26, v26
	v_exp_f32_e32 v27, v27
	v_cvt_pk_f16_f32 v58, v20, v21
	v_cvt_pk_f16_f32 v59, v22, v23
	v_cvt_pk_f16_f32 v90, v24, v25
	v_cvt_pk_f16_f32 v91, v26, v27
	v_add_f32_e32 v16, 0x42c00000, v2
	v_add_f32_e32 v17, 0x42c20000, v2
	v_add_f32_e32 v18, 0x42c40000, v2
	v_add_f32_e32 v19, 0x42c60000, v2
	v_mul_f32_e32 v16, v16, v16
	v_mul_f32_e32 v17, v17, v17
	v_mul_f32_e32 v18, v18, v18
	v_mul_f32_e32 v19, v19, v19
	v_mul_f32_e32 v20, v28, v16
	v_mul_f32_e32 v24, v29, v16
	v_mul_f32_e32 v21, v28, v17
	v_mul_f32_e32 v25, v29, v17
	v_mul_f32_e32 v22, v28, v18
	v_mul_f32_e32 v26, v29, v18
	v_mul_f32_e32 v23, v28, v19
	v_mul_f32_e32 v27, v29, v19
	v_exp_f32_e32 v20, v20
	v_exp_f32_e32 v21, v21
	v_exp_f32_e32 v22, v22
	v_exp_f32_e32 v23, v23
	v_exp_f32_e32 v24, v24
	v_exp_f32_e32 v25, v25
	v_exp_f32_e32 v26, v26
	v_exp_f32_e32 v27, v27
	v_cvt_pk_f16_f32 v60, v20, v21
	v_cvt_pk_f16_f32 v61, v22, v23
	v_cvt_pk_f16_f32 v92, v24, v25
	v_cvt_pk_f16_f32 v93, v26, v27
	v_add_f32_e32 v16, 0x42c80000, v2
	v_add_f32_e32 v17, 0x42ca0000, v2
	v_add_f32_e32 v18, 0x42cc0000, v2
	v_add_f32_e32 v19, 0x42ce0000, v2
	v_mul_f32_e32 v16, v16, v16
	v_mul_f32_e32 v17, v17, v17
	v_mul_f32_e32 v18, v18, v18
	v_mul_f32_e32 v19, v19, v19
	v_mul_f32_e32 v20, v28, v16
	v_mul_f32_e32 v24, v29, v16
	v_mul_f32_e32 v21, v28, v17
	v_mul_f32_e32 v25, v29, v17
	v_mul_f32_e32 v22, v28, v18
	v_mul_f32_e32 v26, v29, v18
	v_mul_f32_e32 v23, v28, v19
	v_mul_f32_e32 v27, v29, v19
	v_exp_f32_e32 v20, v20
	v_exp_f32_e32 v21, v21
	v_exp_f32_e32 v22, v22
	v_exp_f32_e32 v23, v23
	v_exp_f32_e32 v24, v24
	v_exp_f32_e32 v25, v25
	v_exp_f32_e32 v26, v26
	v_exp_f32_e32 v27, v27
	v_cvt_pk_f16_f32 v62, v20, v21
	v_cvt_pk_f16_f32 v63, v22, v23
	v_cvt_pk_f16_f32 v94, v24, v25
	v_cvt_pk_f16_f32 v95, v26, v27
	v_add_u32_e32 v6, 0x8000, v6
	global_load_dwordx4 v[208:211], v6, s[12:13] offset:0 nt
	global_load_dwordx4 v[212:215], v6, s[12:13] offset:1024 nt
	global_load_dwordx4 v[216:219], v6, s[12:13] offset:2048 nt
	global_load_dwordx4 v[220:223], v6, s[12:13] offset:3072 nt
	v_mul_f32_e32 v16, v13, v13
	v_add_f32_e32 v17, 0x3f800000, v13
	v_add_f32_e32 v18, 0x40000000, v13
	v_add_f32_e32 v19, 0x40400000, v13
	v_mul_f32_e32 v17, v17, v17
	v_mul_f32_e32 v18, v18, v18
	v_mul_f32_e32 v19, v19, v19
	v_mul_f32_e32 v20, v8, v16
	v_mul_f32_e32 v24, v9, v16
	v_mul_f32_e32 v21, v8, v17
	v_mul_f32_e32 v25, v9, v17
	v_mul_f32_e32 v22, v8, v18
	v_mul_f32_e32 v26, v9, v18
	v_mul_f32_e32 v23, v8, v19
	v_mul_f32_e32 v27, v9, v19
	v_exp_f32_e32 v20, v20
	v_exp_f32_e32 v21, v21
	v_exp_f32_e32 v22, v22
	v_exp_f32_e32 v23, v23
	v_exp_f32_e32 v24, v24
	v_exp_f32_e32 v25, v25
	v_exp_f32_e32 v26, v26
	v_exp_f32_e32 v27, v27
	v_mul_f32_e32 v96, v10, v20
	v_mul_f32_e32 v97, v10, v21
	v_mul_f32_e32 v98, v10, v22
	v_mul_f32_e32 v99, v10, v23
	v_mul_f32_e32 v112, v11, v24
	v_mul_f32_e32 v113, v11, v25
	v_mul_f32_e32 v114, v11, v26
	v_mul_f32_e32 v115, v11, v27
	v_add_f32_e32 v16, 0x41800000, v13
	v_add_f32_e32 v17, 0x41880000, v13
	v_add_f32_e32 v18, 0x41900000, v13
	v_add_f32_e32 v19, 0x41980000, v13
	v_mul_f32_e32 v16, v16, v16
	v_mul_f32_e32 v17, v17, v17
	v_mul_f32_e32 v18, v18, v18
	v_mul_f32_e32 v19, v19, v19
	v_mul_f32_e32 v20, v8, v16
	v_mul_f32_e32 v24, v9, v16
	v_mul_f32_e32 v21, v8, v17
	v_mul_f32_e32 v25, v9, v17
	v_mul_f32_e32 v22, v8, v18
	v_mul_f32_e32 v26, v9, v18
	v_mul_f32_e32 v23, v8, v19
	v_mul_f32_e32 v27, v9, v19
	v_exp_f32_e32 v20, v20
	v_exp_f32_e32 v21, v21
	v_exp_f32_e32 v22, v22
	v_exp_f32_e32 v23, v23
	v_exp_f32_e32 v24, v24
	v_exp_f32_e32 v25, v25
	v_exp_f32_e32 v26, v26
	v_exp_f32_e32 v27, v27
	v_mul_f32_e32 v100, v10, v20
	v_mul_f32_e32 v101, v10, v21
	v_mul_f32_e32 v102, v10, v22
	v_mul_f32_e32 v103, v10, v23
	v_mul_f32_e32 v116, v11, v24
	v_mul_f32_e32 v117, v11, v25
	v_mul_f32_e32 v118, v11, v26
	v_mul_f32_e32 v119, v11, v27
	v_add_u32_e32 v6, 0x8000, v6
	global_load_dwordx4 v[224:227], v6, s[12:13] offset:0 nt
	global_load_dwordx4 v[228:231], v6, s[12:13] offset:1024 nt
	global_load_dwordx4 v[232:235], v6, s[12:13] offset:2048 nt
	global_load_dwordx4 v[236:239], v6, s[12:13] offset:3072 nt
	v_mul_f32_e32 v16, v3, v3
	v_add_f32_e32 v17, 0x3f800000, v3
	v_add_f32_e32 v18, 0x40000000, v3
	v_add_f32_e32 v19, 0x40400000, v3
	v_mul_f32_e32 v17, v17, v17
	v_mul_f32_e32 v18, v18, v18
	v_mul_f32_e32 v19, v19, v19
	v_mul_f32_e32 v20, v28, v16
	v_mul_f32_e32 v24, v29, v16
	v_mul_f32_e32 v21, v28, v17
	v_mul_f32_e32 v25, v29, v17
	v_mul_f32_e32 v22, v28, v18
	v_mul_f32_e32 v26, v29, v18
	v_mul_f32_e32 v23, v28, v19
	v_mul_f32_e32 v27, v29, v19
	v_exp_f32_e32 v20, v20
	v_exp_f32_e32 v21, v21
	v_exp_f32_e32 v22, v22
	v_exp_f32_e32 v23, v23
	v_exp_f32_e32 v24, v24
	v_exp_f32_e32 v25, v25
	v_exp_f32_e32 v26, v26
	v_exp_f32_e32 v27, v27
	v_mul_f32_e32 v104, v30, v20
	v_mul_f32_e32 v105, v30, v21
	v_mul_f32_e32 v106, v30, v22
	v_mul_f32_e32 v107, v30, v23
	v_mul_f32_e32 v120, v31, v24
	v_mul_f32_e32 v121, v31, v25
	v_mul_f32_e32 v122, v31, v26
	v_mul_f32_e32 v123, v31, v27
	v_add_f32_e32 v16, 0x41800000, v3
	v_add_f32_e32 v17, 0x41880000, v3
	v_add_f32_e32 v18, 0x41900000, v3
	v_add_f32_e32 v19, 0x41980000, v3
	v_mul_f32_e32 v16, v16, v16
	v_mul_f32_e32 v17, v17, v17
	v_mul_f32_e32 v18, v18, v18
	v_mul_f32_e32 v19, v19, v19
	v_mul_f32_e32 v20, v28, v16
	v_mul_f32_e32 v24, v29, v16
	v_mul_f32_e32 v21, v28, v17
	v_mul_f32_e32 v25, v29, v17
	v_mul_f32_e32 v22, v28, v18
	v_mul_f32_e32 v26, v29, v18
	v_mul_f32_e32 v23, v28, v19
	v_mul_f32_e32 v27, v29, v19
	v_exp_f32_e32 v20, v20
	v_exp_f32_e32 v21, v21
	v_exp_f32_e32 v22, v22
	v_exp_f32_e32 v23, v23
	v_exp_f32_e32 v24, v24
	v_exp_f32_e32 v25, v25
	v_exp_f32_e32 v26, v26
	v_exp_f32_e32 v27, v27
	v_mul_f32_e32 v108, v30, v20
	v_mul_f32_e32 v109, v30, v21
	v_mul_f32_e32 v110, v30, v22
	v_mul_f32_e32 v111, v30, v23
	v_mul_f32_e32 v124, v31, v24
	v_mul_f32_e32 v125, v31, v25
	v_mul_f32_e32 v126, v31, v26
	v_mul_f32_e32 v127, v31, v27
	v_add_u32_e32 v6, 0x8000, v6
	global_load_dwordx4 v[240:243], v6, s[12:13] offset:0 nt
	global_load_dwordx4 v[244:247], v6, s[12:13] offset:1024 nt
	global_load_dwordx4 v[248:251], v6, s[12:13] offset:2048 nt
	global_load_dwordx4 v[252:255], v6, s[12:13] offset:3072 nt
	s_waitcnt vmcnt(28)
	v_add_f32_e32 v128, v128, v129
	v_add_f32_e32 v130, v130, v131
	v_add_f32_e32 v132, v132, v133
	v_add_f32_e32 v134, v134, v135
	v_add_f32_e32 v136, v136, v137
	v_add_f32_e32 v138, v138, v139
	v_add_f32_e32 v140, v140, v141
	v_add_f32_e32 v142, v142, v143
	v_add_f32_e32 v128, v128, v130
	v_add_f32_e32 v132, v132, v134
	v_add_f32_e32 v136, v136, v138
	v_add_f32_e32 v140, v140, v142
	v_cndmask_b32_e64 v130, v128, v132, s[30:31]
	v_cndmask_b32_e64 v134, v136, v140, s[30:31]
	v_cndmask_b32_e64 v129, v132, v128, s[30:31]
	v_cndmask_b32_e64 v133, v140, v136, s[30:31]
	v_add_f32_dpp v129, v130, v129 quad_perm:[1,0,3,2] row_mask:0xf bank_mask:0xf bound_ctrl:1
	v_add_f32_dpp v133, v134, v133 quad_perm:[1,0,3,2] row_mask:0xf bank_mask:0xf bound_ctrl:1
	v_cndmask_b32_e64 v135, v129, v133, s[32:33]
	v_cndmask_b32_e64 v131, v133, v129, s[32:33]
	s_nop 1
	v_add_f32_dpp v131, v135, v131 quad_perm:[2,3,0,1] row_mask:0xf bank_mask:0xf bound_ctrl:1
	v_cvt_f16_f32_e32 v131, v131
	ds_write_b16 v14, v131 offset:0
	s_waitcnt vmcnt(24)
	v_add_f32_e32 v144, v144, v145
	v_add_f32_e32 v146, v146, v147
	v_add_f32_e32 v148, v148, v149
	v_add_f32_e32 v150, v150, v151
	v_add_f32_e32 v152, v152, v153
	v_add_f32_e32 v154, v154, v155
	v_add_f32_e32 v156, v156, v157
	v_add_f32_e32 v158, v158, v159
	v_add_f32_e32 v144, v144, v146
	v_add_f32_e32 v148, v148, v150
	v_add_f32_e32 v152, v152, v154
	v_add_f32_e32 v156, v156, v158
	v_cndmask_b32_e64 v146, v144, v148, s[30:31]
	v_cndmask_b32_e64 v150, v152, v156, s[30:31]
	v_cndmask_b32_e64 v145, v148, v144, s[30:31]
	v_cndmask_b32_e64 v149, v156, v152, s[30:31]
	v_add_f32_dpp v145, v146, v145 quad_perm:[1,0,3,2] row_mask:0xf bank_mask:0xf bound_ctrl:1
	v_add_f32_dpp v149, v150, v149 quad_perm:[1,0,3,2] row_mask:0xf bank_mask:0xf bound_ctrl:1
	v_cndmask_b32_e64 v151, v145, v149, s[32:33]
	v_cndmask_b32_e64 v147, v149, v145, s[32:33]
	s_nop 1
	v_add_f32_dpp v147, v151, v147 quad_perm:[2,3,0,1] row_mask:0xf bank_mask:0xf bound_ctrl:1
	v_cvt_f16_f32_e32 v147, v147
	ds_write_b16 v14, v147 offset:1088
	s_waitcnt vmcnt(20)
	v_add_f32_e32 v160, v160, v161
	v_add_f32_e32 v162, v162, v163
	v_add_f32_e32 v164, v164, v165
	v_add_f32_e32 v166, v166, v167
	v_add_f32_e32 v168, v168, v169
	v_add_f32_e32 v170, v170, v171
	v_add_f32_e32 v172, v172, v173
	v_add_f32_e32 v174, v174, v175
	v_add_f32_e32 v160, v160, v162
	v_add_f32_e32 v164, v164, v166
	v_add_f32_e32 v168, v168, v170
	v_add_f32_e32 v172, v172, v174
	v_cndmask_b32_e64 v162, v160, v164, s[30:31]
	v_cndmask_b32_e64 v166, v168, v172, s[30:31]
	v_cndmask_b32_e64 v161, v164, v160, s[30:31]
	v_cndmask_b32_e64 v165, v172, v168, s[30:31]
	v_add_f32_dpp v161, v162, v161 quad_perm:[1,0,3,2] row_mask:0xf bank_mask:0xf bound_ctrl:1
	v_add_f32_dpp v165, v166, v165 quad_perm:[1,0,3,2] row_mask:0xf bank_mask:0xf bound_ctrl:1
	v_cndmask_b32_e64 v167, v161, v165, s[32:33]
	v_cndmask_b32_e64 v163, v165, v161, s[32:33]
	s_nop 1
	v_add_f32_dpp v163, v167, v163 quad_perm:[2,3,0,1] row_mask:0xf bank_mask:0xf bound_ctrl:1
	v_cvt_f16_f32_e32 v163, v163
	ds_write_b16 v14, v163 offset:2176
	s_waitcnt vmcnt(16)
	v_add_f32_e32 v176, v176, v177
	v_add_f32_e32 v178, v178, v179
	v_add_f32_e32 v180, v180, v181
	v_add_f32_e32 v182, v182, v183
	v_add_f32_e32 v184, v184, v185
	v_add_f32_e32 v186, v186, v187
	v_add_f32_e32 v188, v188, v189
	v_add_f32_e32 v190, v190, v191
	v_add_f32_e32 v176, v176, v178
	v_add_f32_e32 v180, v180, v182
	v_add_f32_e32 v184, v184, v186
	v_add_f32_e32 v188, v188, v190
	v_cndmask_b32_e64 v178, v176, v180, s[30:31]
	v_cndmask_b32_e64 v182, v184, v188, s[30:31]
	v_cndmask_b32_e64 v177, v180, v176, s[30:31]
	v_cndmask_b32_e64 v181, v188, v184, s[30:31]
	v_add_f32_dpp v177, v178, v177 quad_perm:[1,0,3,2] row_mask:0xf bank_mask:0xf bound_ctrl:1
	v_add_f32_dpp v181, v182, v181 quad_perm:[1,0,3,2] row_mask:0xf bank_mask:0xf bound_ctrl:1
	v_cndmask_b32_e64 v183, v177, v181, s[32:33]
	v_cndmask_b32_e64 v179, v181, v177, s[32:33]
	s_nop 1
	v_add_f32_dpp v179, v183, v179 quad_perm:[2,3,0,1] row_mask:0xf bank_mask:0xf bound_ctrl:1
	v_cvt_f16_f32_e32 v179, v179
	ds_write_b16 v14, v179 offset:3264
	s_mov_b32 s29, 0
	v_mov_b32_e32 v22, 0
	v_mov_b32_e32 v23, 0
	v_mov_b32_e32 v24, 0
	v_mov_b32_e32 v25, 0
	s_lshl_b32 s6, s6, 6
	s_add_i32 s6, s6, s7
	s_lshl_b32 s6, s6, 10
	v_add_u32_e32 v5, s6, v5
	s_branch .Lpass

.Lpass:
	s_waitcnt lgkmcnt(0)
	s_barrier
	ds_read_b128 v[176:179], v15 offset:0
	ds_read_b128 v[180:183], v15 offset:64
	ds_read_b128 v[184:187], v15 offset:128
	ds_read_b128 v[188:191], v15 offset:192
	s_waitcnt lgkmcnt(3)
	v_mfma_f32_16x16x32_f16 v[160:163], v[176:179], v[32:35], 0
	v_mfma_f32_16x16x32_f16 v[168:171], v[176:179], v[64:67], 0
	v_mfma_f32_16x16x32_f16 v[164:167], v[176:179], v[48:51], 0
	v_mfma_f32_16x16x32_f16 v[172:175], v[176:179], v[80:83], 0
	s_waitcnt lgkmcnt(2)
	v_mfma_f32_16x16x32_f16 v[160:163], v[180:183], v[36:39], v[160:163]
	v_mfma_f32_16x16x32_f16 v[168:171], v[180:183], v[68:71], v[168:171]
	v_mfma_f32_16x16x32_f16 v[164:167], v[180:183], v[52:55], v[164:167]
	v_mfma_f32_16x16x32_f16 v[172:175], v[180:183], v[84:87], v[172:175]
	s_waitcnt lgkmcnt(1)
	v_mfma_f32_16x16x32_f16 v[160:163], v[184:187], v[40:43], v[160:163]
	v_mfma_f32_16x16x32_f16 v[168:171], v[184:187], v[72:75], v[168:171]
	v_mfma_f32_16x16x32_f16 v[164:167], v[184:187], v[56:59], v[164:167]
	v_mfma_f32_16x16x32_f16 v[172:175], v[184:187], v[88:91], v[172:175]
	s_waitcnt lgkmcnt(0)
	v_mfma_f32_16x16x32_f16 v[160:163], v[188:191], v[44:47], v[160:163]
	v_mfma_f32_16x16x32_f16 v[168:171], v[188:191], v[76:79], v[168:171]
	v_mfma_f32_16x16x32_f16 v[164:167], v[188:191], v[60:63], v[164:167]
	v_mfma_f32_16x16x32_f16 v[172:175], v[188:191], v[92:95], v[172:175]
	s_nop 15
	v_fma_f32 v22, v96, v160, v22
	v_fma_f32 v23, -v112, v168, v23
	v_fma_f32 v24, v104, v164, v24
	v_fma_f32 v25, -v120, v172, v25
	v_fma_f32 v22, v97, v161, v22
	v_fma_f32 v23, -v113, v169, v23
	v_fma_f32 v24, v105, v165, v24
	v_fma_f32 v25, -v121, v173, v25
	v_fma_f32 v22, v98, v162, v22
	v_fma_f32 v23, -v114, v170, v23
	v_fma_f32 v24, v106, v166, v24
	v_fma_f32 v25, -v122, v174, v25
	v_fma_f32 v22, v99, v163, v22
	v_fma_f32 v23, -v115, v171, v23
	v_fma_f32 v24, v107, v167, v24
	v_fma_f32 v25, -v123, v175, v25
	v_add_f32_e32 v26, v22, v23
	v_add_f32_e32 v27, v24, v25
	v_cmp_gt_u32_e32 vcc, 32, v1
	s_cmp_eq_u32 s29, 1
	v_permlane16_swap_b32_e32 v26, v27
	s_nop 0
	v_add_f32_e32 v26, v26, v27
	v_mov_b32_e32 v27, v26
	s_nop 1
	v_permlane32_swap_b32_e32 v26, v27
	s_nop 0
	v_add_f32_e32 v26, v26, v27
	s_cbranch_scc1 .Lstore
	s_cmp_eq_u32 s29, 2
	s_cbranch_scc1 .Ldry_done
	s_mov_b32 s29, 1
	v_add_u32_e32 v15, 0x1100, v15
	v_mov_b32_e32 v96, v100
	v_mov_b32_e32 v112, v116
	v_mov_b32_e32 v97, v101
	v_mov_b32_e32 v113, v117
	v_mov_b32_e32 v98, v102
	v_mov_b32_e32 v114, v118
	v_mov_b32_e32 v99, v103
	v_mov_b32_e32 v115, v119
	v_mov_b32_e32 v104, v108
	v_mov_b32_e32 v120, v124
	v_mov_b32_e32 v105, v109
	v_mov_b32_e32 v121, v125
	v_mov_b32_e32 v106, v110
	v_mov_b32_e32 v122, v126
	v_mov_b32_e32 v107, v111
	v_mov_b32_e32 v123, v127
	s_branch .Lsecond_half
.Lstore:
	s_and_saveexec_b64 s[2:3], vcc
	s_cbranch_execz .Ldog_main_done
	global_store_dword v5, v26, s[26:27]

	.amdhsa_kernel _Z7dog_finPKfS0_Pf
		.amdhsa_group_segment_fixed_size 0
		.amdhsa_private_segment_fixed_size 0
		.amdhsa_kernarg_size 24
		.amdhsa_user_sgpr_count 2
		.amdhsa_user_sgpr_dispatch_ptr 0
		.amdhsa_user_sgpr_queue_ptr 0
		.amdhsa_user_sgpr_kernarg_segment_ptr 1
		.amdhsa_user_sgpr_dispatch_id 0
		.amdhsa_user_sgpr_kernarg_preload_length 0
		.amdhsa_user_sgpr_kernarg_preload_offset 0
		.amdhsa_user_sgpr_private_segment_size 0
		.amdhsa_uses_dynamic_stack 0
		.amdhsa_enable_private_segment 0
		.amdhsa_system_sgpr_workgroup_id_x 1
		.amdhsa_system_sgpr_workgroup_id_y 0
		.amdhsa_system_sgpr_workgroup_id_z 0
		.amdhsa_system_sgpr_workgroup_info 0
		.amdhsa_system_vgpr_workitem_id 0
		.amdhsa_next_free_vgpr 16
		.amdhsa_next_free_sgpr 20
		.amdhsa_accum_offset 16
		.amdhsa_reserve_vcc 1
		.amdhsa_float_round_mode_32 0
		.amdhsa_float_round_mode_16_64 0
		.amdhsa_float_denorm_mode_32 3
		.amdhsa_float_denorm_mode_16_64 3
		.amdhsa_dx10_clamp 1
		.amdhsa_ieee_mode 1
		.amdhsa_fp16_overflow 0
		.amdhsa_tg_split 0
		.amdhsa_exception_fp_ieee_invalid_op 0
		.amdhsa_exception_fp_denorm_src 0
		.amdhsa_exception_fp_ieee_div_zero 0
		.amdhsa_exception_fp_ieee_overflow 0
		.amdhsa_exception_fp_ieee_underflow 0
		.amdhsa_exception_fp_ieee_inexact 0
		.amdhsa_exception_int_div_zero 0
	.end_amdhsa_kernel
